# gdnout2: the four z-gate loads of a unit issued as soon as their addresses exist (two barriers earlier) into registers that are dead in that window, copied into place behind the waits
# speedup vs baseline: 1.0113x; 1.0113x over previous
; #define LAS __attribute__((address_space(3)))
; DI float bflo(unsigned u) { return __uint_as_float(u << 16); }
; DI void gdn_out_unit(const Params& p, int U, char* lds) {
;     ...
;   const char* wfg = (const char*)(p.ws + WS_WF) + (size_t)U * 16384 + lane * 16;
;   const char* qfg = (const char*)p.out + (size_t)U * 16384 + lane * 16;
;   const char* afg = (const char*)p.out + 64 * MiB + (size_t)U * 8192 + lane * 16;
;   const bf16_t* UF = (const bf16_t*)(p.ws + WS_UF) + (size_t)U * 8192;
;   const bf16x8* SC = (const bf16x8*)(p.ws + WS_SC + (size_t)U * 32768 + (size_t)wv * 8192) + lane;
;   bf16_t* ol = (bf16_t*)(lds + 40960);
;   __syncthreads();
; #pragma unroll
;   for (int i = 0; i < 4; ++i) {
;     __builtin_amdgcn_global_load_lds((const unsigned*)(wfg + (4 * wv + i) * 1024), (LAS unsigned*)(lds + (4 * wv + i) * 1024), 16, 0, 0);
;     __builtin_amdgcn_global_load_lds((const unsigned*)(qfg + (4 * wv + i) * 1024), (LAS unsigned*)(lds + 16384 + (4 * wv + i) * 1024), 16, 0, 0);
;   }
; #pragma unroll
;   for (int i = 0; i < 2; ++i) __builtin_amdgcn_global_load_lds((const unsigned*)(afg + (2 * wv + i) * 1024), (LAS unsigned*)(lds + 32768 + (2 * wv + i) * 1024), 16, 0, 0);
;   bf16x8 Sb[4][2];
; #pragma unroll
;   for (int m = 0; m < 4; ++m) { Sb[m][0] = SC[(m * 2 + 0) * 64]; Sb[m][1] = SC[(m * 2 + 1) * 64]; }
;   u32x4 uu[4];
; #pragma unroll
;   for (int i2 = 0; i2 < 2; ++i2) { uu[2 * i2] = *(const u32x4*)(UF + (size_t)((i2 * 4 + wv) * 64 + lane) * 16); uu[2 * i2 + 1] = *(const u32x4*)(UF + (size_t)((i2 * 4 + wv) * 64 + lane) * 16 + 8); }
;   __syncthreads();
;   const char* lw = lds + lane * 16; const char* lq = lds + 16384 + lane * 16; const char* la = lds + 32768 + lane * 16;
;   f32x16 vn[2], o[2];
; #pragma unroll
;   for (int i2 = 0; i2 < 2; ++i2) {
; #pragma unroll
;     for (int e = 0; e < 4; ++e) { vn[i2][2 * e] = bflo(uu[2 * i2][e]); vn[i2][2 * e + 1] = bfhi(uu[2 * i2][e]); vn[i2][8 + 2 * e] = bflo(uu[2 * i2 + 1][e]); vn[i2][8 + 2 * e + 1] = bfhi(uu[2 * i2 + 1][e]); }
; #pragma unroll
;     for (int r = 0; r < 16; ++r) o[i2][r] = 0.f;
; #pragma unroll
;     for (int m = 0; m < 4; ++m)
; #pragma unroll
;       for (int s = 0; s < 2; ++s) {
;         vn[i2] = MFMA32(*(const bf16x8*)(lw + ((i2 * 4 + m) * 2 + s) * 1024), Sb[m][s], vn[i2]);
;         o[i2] = MFMA32(*(const bf16x8*)(lq + ((i2 * 4 + m) * 2 + s) * 1024), Sb[m][s], o[i2]);
;       }
;   }
.LBB0_1336:
	v_mov_b32_e32 v86, v206
	s_nop 0
	v_ashrrev_i32_e32 v0, 6, v86
	v_ashrrev_i32_e32 v87, 31, v86
	v_lshlrev_b32_e32 v1, 4, v86
	v_add_u32_e32 v2, 0x100, v86
	v_lshlrev_b32_e32 v8, 12, v0
	v_lshlrev_b64 v[4:5], 5, v[86:87]
	v_and_b32_e32 v10, 0x3f0, v1
	v_ashrrev_i32_e32 v3, 31, v2
	v_add_u32_e32 v12, v146, v8
	v_lshl_add_u64 v[4:5], v[80:81], 0, v[4:5]
	v_ashrrev_i32_e32 v1, 31, v0
	v_lshlrev_b32_e32 v11, 11, v0
	v_ashrrev_i32_e32 v7, 31, v8
	v_or_b32_e32 v6, v8, v10
	v_lshlrev_b64 v[2:3], 5, v[2:3]
	v_add_u32_e32 v16, 0x4400, v12
	v_add_u32_e32 v17, 0x800, v12
	v_lshl_add_u64 v[4:5], s[84:85], 0, v[4:5]
	v_lshlrev_b64 v[0:1], 13, v[0:1]
	v_ashrrev_i32_e32 v9, 31, v11
	v_or_b32_e32 v8, v11, v10
	v_add_u32_e32 v11, v146, v11
	v_lshl_add_u64 v[6:7], v[80:81], 0, v[6:7]
	v_lshl_add_u64 v[2:3], v[80:81], 0, v[2:3]
	v_readfirstlane_b32 s60, v16
	v_readfirstlane_b32 s61, v17
	v_lshl_add_u64 v[16:17], v[4:5], 0, s[38:39]
	v_add_co_u32_e32 v4, vcc, s19, v4
	v_add_u32_e32 v87, v146, v10
	v_or_b32_e32 v0, v0, v10
	v_readfirstlane_b32 s49, v12
	v_add_u32_e32 v14, 0x4000, v12
	v_add_u32_e32 v15, 0x400, v12
	v_add_u32_e32 v18, 0x4800, v12
	v_add_u32_e32 v19, 0xc00, v12
	v_add_u32_e32 v20, 0x4c00, v12
	v_add_u32_e32 v21, 0x8000, v11
	v_add_u32_e32 v22, 0x8400, v11
	v_lshl_add_u64 v[10:11], s[84:85], 0, v[6:7]
	v_lshl_add_u64 v[12:13], s[66:67], 0, v[6:7]
	v_addc_co_u32_e32 v5, vcc, 0, v5, vcc
	v_lshl_add_u64 v[6:7], s[84:85], 0, v[2:3]
	v_lshl_add_u64 v[0:1], v[76:77], 0, v[0:1]
	v_add_co_u32_e32 v36, vcc, s19, v6
	v_readfirstlane_b32 s68, v18
	v_readfirstlane_b32 s69, v19
	v_readfirstlane_b32 s70, v20
	v_readfirstlane_b32 s71, v21
	v_lshl_add_u64 v[18:19], s[84:85], 0, v[0:1]
	v_lshl_add_u64 v[20:21], v[10:11], 0, s[12:13]
	v_addc_co_u32_e32 v37, vcc, 0, v7, vcc
	s_mov_b32 m0, s49
	s_barrier
	global_load_lds_dwordx4 v[20:21], off
	v_add_co_u32_e32 v20, vcc, s3, v18
	global_load_dwordx4 v[0:3], v[4:5], off
	s_nop 0
	v_addc_co_u32_e32 v21, vcc, 0, v19, vcc
	v_add_co_u32_e32 v18, vcc, s18, v18
	v_lshl_add_u64 v[4:5], v[6:7], 0, s[38:39]
	s_nop 0
	v_addc_co_u32_e32 v19, vcc, 0, v19, vcc
	global_load_dwordx4 v[4:7], v[4:5], off offset:16
	s_nop 0
	global_load_dwordx4 v[92:95], v[18:19], off offset:-4096
	global_load_dwordx4 v[32:35], v[16:17], off offset:16
	s_nop 0
	global_load_dwordx4 v[36:39], v[36:37], off
	s_nop 0
	global_load_dwordx4 v[96:99], v[20:21], off offset:3072
	v_readfirstlane_b32 s50, v14
	s_mov_b32 m0, s50
	v_readfirstlane_b32 s51, v15
	global_load_lds_dwordx4 v[12:13], off
	global_load_dwordx4 v[100:103], v[20:21], off offset:1024
	global_load_dwordx4 v[104:107], v[20:21], off offset:2048
	global_load_dwordx4 v[108:111], v[18:19], off
	global_load_dwordx4 v[72:75], v[18:19], off offset:1024
	global_load_dwordx4 v[68:71], v[18:19], off offset:2048
	global_load_dwordx4 v[64:67], v[18:19], off offset:3072
	v_readfirstlane_b32 s72, v22
	v_lshl_add_u64 v[22:23], v[10:11], 0, s[14:15]
	s_mov_b32 m0, s51
	v_lshl_add_u64 v[24:25], v[12:13], 0, s[16:17]
	global_load_lds_dwordx4 v[22:23], off
	s_mov_b32 m0, s60
	v_lshl_add_u64 v[26:27], v[10:11], 0, s[24:25]
	global_load_lds_dwordx4 v[24:25], off
	s_mov_b32 m0, s61
	v_lshl_add_u64 v[28:29], v[12:13], 0, s[26:27]
	global_load_lds_dwordx4 v[26:27], off
	s_mov_b32 m0, s68
	v_lshl_add_u64 v[10:11], v[10:11], 0, s[28:29]
	global_load_lds_dwordx4 v[28:29], off
	s_mov_b32 m0, s69
	v_lshl_add_u64 v[8:9], v[78:79], 0, v[8:9]
	v_lshl_add_u64 v[30:31], v[12:13], 0, s[30:31]
	global_load_lds_dwordx4 v[10:11], off
	s_mov_b32 m0, s70
	v_lshl_add_u64 v[14:15], v[8:9], 0, s[34:35]
	global_load_lds_dwordx4 v[30:31], off
	s_mov_b32 m0, s71
	v_and_b32_e32 v91, 31, v86
	global_load_lds_dwordx4 v[14:15], off
	s_mov_b32 m0, s72
	v_and_b32_e32 v84, 0x180, v90
	global_load_lds_dwordx4 v[8:9], off
	s_waitcnt vmcnt(0) lgkmcnt(0)
	s_barrier
	ds_read_b128 v[112:115], v87
	ds_read_b128 v[116:119], v87 offset:1024
	ds_read_b128 v[8:11], v87 offset:16384
	ds_read_b128 v[120:123], v87 offset:17408
	ds_read_b128 v[124:127], v87 offset:8192
	ds_read_b128 v[128:131], v87 offset:9216
	ds_read_b128 v[12:15], v87 offset:24576
	ds_read_b128 v[132:135], v87 offset:25600
	s_waitcnt lgkmcnt(5)
	v_mfma_f32_32x32x16_bf16 v[16:31], v[8:11], v[92:95], 0
	v_lshlrev_b32_e32 v48, 16, v0
	v_and_b32_e32 v49, 0xffff0000, v0
	v_lshlrev_b32_e32 v50, 16, v1
	v_and_b32_e32 v51, 0xffff0000, v1
	v_lshlrev_b32_e32 v52, 16, v2
	v_and_b32_e32 v53, 0xffff0000, v2
	v_lshlrev_b32_e32 v54, 16, v3
	v_and_b32_e32 v55, 0xffff0000, v3
	v_lshlrev_b32_e32 v40, 16, v4
	v_and_b32_e32 v41, 0xffff0000, v4
	v_lshlrev_b32_e32 v42, 16, v5
	v_and_b32_e32 v43, 0xffff0000, v5
	v_lshlrev_b32_e32 v44, 16, v6
	v_and_b32_e32 v45, 0xffff0000, v6
	v_lshlrev_b32_e32 v46, 16, v7
	v_and_b32_e32 v47, 0xffff0000, v7
	v_lshlrev_b32_e32 v56, 16, v32
	v_and_b32_e32 v57, 0xffff0000, v32
	v_lshlrev_b32_e32 v58, 16, v33
	v_and_b32_e32 v59, 0xffff0000, v33
	v_lshlrev_b32_e32 v60, 16, v34
	v_and_b32_e32 v61, 0xffff0000, v34
	v_lshlrev_b32_e32 v62, 16, v35
	v_and_b32_e32 v63, 0xffff0000, v35
	v_lshlrev_b32_e32 v32, 16, v36
	v_and_b32_e32 v33, 0xffff0000, v36
	v_lshlrev_b32_e32 v34, 16, v37
	v_and_b32_e32 v35, 0xffff0000, v37
	v_lshlrev_b32_e32 v36, 16, v38
	v_and_b32_e32 v37, 0xffff0000, v38
	v_lshlrev_b32_e32 v38, 16, v39
	v_and_b32_e32 v39, 0xffff0000, v39
	s_waitcnt lgkmcnt(1)
	v_mfma_f32_32x32x16_bf16 v[0:15], v[12:15], v[92:95], 0
	v_lshlrev_b32_e32 v84, 1, v84
	v_lshl_add_u64 v[78:79], v[78:79], 0, s[6:7]
	v_lshl_add_u64 v[80:81], v[80:81], 0, s[8:9]
	v_lshl_add_u64 v[76:77], v[76:77], 0, s[4:5]
	v_mfma_f32_32x32x16_bf16 v[48:63], v[112:115], v[92:95], v[48:63]
	v_mfma_f32_32x32x16_bf16 v[32:47], v[124:127], v[92:95], v[32:47]
	v_mfma_f32_32x32x16_bf16 v[16:31], v[120:123], v[100:103], v[16:31]
	s_waitcnt lgkmcnt(0)
; DI float bflo(unsigned u) { return __uint_as_float(u << 16); }
; DI float bfhi(unsigned u) { return __uint_as_float(u & 0xffff0000u); }
; #define MFMA32(a, b, c) __builtin_amdgcn_mfma_f32_32x32x16_bf16((a), (b), (c), 0, 0, 0)
; DI bf16x8 packS(const f32x16& x, int s) { return pack8(x[8 * s], x[8 * s + 1], x[8 * s + 2], x[8 * s + 3], x[8 * s + 4], x[8 * s + 5], x[8 * s + 6], x[8 * s + 7]); }
; DI void gdn_out_unit(const Params& p, int U, char* lds) {
;     ...
;   for (int i2 = 0; i2 < 2; ++i2) {
; #pragma unroll
;     for (int e = 0; e < 4; ++e) { vn[i2][2 * e] = bflo(uu[2 * i2][e]); vn[i2][2 * e + 1] = bfhi(uu[2 * i2][e]); vn[i2][8 + 2 * e] = bflo(uu[2 * i2 + 1][e]); vn[i2][8 + 2 * e + 1] = bfhi(uu[2 * i2 + 1][e]); }
; #pragma unroll
;     for (int r = 0; r < 16; ++r) o[i2][r] = 0.f;
; #pragma unroll
;     for (int m = 0; m < 4; ++m)
; #pragma unroll
;       for (int s = 0; s < 2; ++s) {
;         vn[i2] = MFMA32(*(const bf16x8*)(lw + ((i2 * 4 + m) * 2 + s) * 1024), Sb[m][s], vn[i2]);
;         o[i2] = MFMA32(*(const bf16x8*)(lq + ((i2 * 4 + m) * 2 + s) * 1024), Sb[m][s], o[i2]);
;       }
;   }
;   bf16x8 Vb[2][2];
; #pragma unroll
;   for (int j2 = 0; j2 < 2; ++j2) { Vb[j2][0] = packS(vn[j2], 0); Vb[j2][1] = packS(vn[j2], 1); }
; #pragma unroll
;   for (int i2 = 0; i2 < 2; ++i2)
; #pragma unroll
;     for (int j2 = 0; j2 <= i2; ++j2)
; #pragma unroll
;       for (int s = 0; s < 2; ++s) o[i2] = MFMA32(*(const bf16x8*)(la + ((i2 * 2 + j2) * 2 + s) * 1024), Vb[j2][s], o[i2]);
;     ...
;     const bf16_t* gzp = proj + (t0 + row) * PP + 3072 + h * 128 + 32 * q4;
;     bf16_t* op = proj + (t0 + row) * PP + 1536 + h * 128 + 32 * q4;
	v_mfma_f32_32x32x16_bf16 v[0:15], v[132:135], v[100:103], v[0:15]
	v_mfma_f32_32x32x16_bf16 v[48:63], v[116:119], v[100:103], v[48:63]
	v_mfma_f32_32x32x16_bf16 v[32:47], v[128:131], v[100:103], v[32:47]
	ds_read_b128 v[92:95], v87 offset:18432
	ds_read_b128 v[100:103], v87 offset:19456
	s_waitcnt lgkmcnt(1)
	v_mfma_f32_32x32x16_bf16 v[16:31], v[92:95], v[104:107], v[16:31]
	ds_read_b128 v[92:95], v87 offset:26624
	ds_read_b128 v[112:115], v87 offset:27648
	s_waitcnt lgkmcnt(1)
	v_mfma_f32_32x32x16_bf16 v[0:15], v[92:95], v[104:107], v[0:15]
	ds_read_b128 v[92:95], v87 offset:2048
	ds_read_b128 v[116:119], v87 offset:3072
	s_waitcnt lgkmcnt(1)
	v_mfma_f32_32x32x16_bf16 v[48:63], v[92:95], v[104:107], v[48:63]
	ds_read_b128 v[92:95], v87 offset:10240
	ds_read_b128 v[120:123], v87 offset:11264
	s_waitcnt lgkmcnt(1)
	v_mfma_f32_32x32x16_bf16 v[32:47], v[92:95], v[104:107], v[32:47]
	v_mfma_f32_32x32x16_bf16 v[16:31], v[100:103], v[96:99], v[16:31]
	v_mfma_f32_32x32x16_bf16 v[0:15], v[112:115], v[96:99], v[0:15]
	v_mfma_f32_32x32x16_bf16 v[48:63], v[116:119], v[96:99], v[48:63]
	s_waitcnt lgkmcnt(0)
	v_mfma_f32_32x32x16_bf16 v[32:47], v[120:123], v[96:99], v[32:47]
	ds_read_b128 v[92:95], v87 offset:20480
	ds_read_b128 v[96:99], v87 offset:21504
	s_waitcnt lgkmcnt(1)
	v_mfma_f32_32x32x16_bf16 v[16:31], v[92:95], v[108:111], v[16:31]
	ds_read_b128 v[92:95], v87 offset:28672
	ds_read_b128 v[100:103], v87 offset:29696
	s_waitcnt lgkmcnt(1)
	v_mfma_f32_32x32x16_bf16 v[0:15], v[92:95], v[108:111], v[0:15]
	ds_read_b128 v[92:95], v87 offset:4096
	ds_read_b128 v[104:107], v87 offset:5120
	s_waitcnt lgkmcnt(1)
	v_mfma_f32_32x32x16_bf16 v[48:63], v[92:95], v[108:111], v[48:63]
	ds_read_b128 v[92:95], v87 offset:12288
	ds_read_b128 v[112:115], v87 offset:13312
	s_waitcnt lgkmcnt(1)
	v_mfma_f32_32x32x16_bf16 v[32:47], v[92:95], v[108:111], v[32:47]
	v_ashrrev_i32_e32 v108, 9, v90
	v_ashrrev_i32_e32 v109, 31, v108
	v_lshrrev_b32_e32 v110, 3, v86
	v_add_u32_e32 v90, s90, v90
	v_mfma_f32_32x32x16_bf16 v[16:31], v[96:99], v[72:75], v[16:31]
	v_mfma_f32_32x32x16_bf16 v[0:15], v[100:103], v[72:75], v[0:15]
	v_mfma_f32_32x32x16_bf16 v[48:63], v[104:107], v[72:75], v[48:63]
	s_waitcnt lgkmcnt(0)
	v_mfma_f32_32x32x16_bf16 v[32:47], v[112:115], v[72:75], v[32:47]
	ds_read_b128 v[72:75], v87 offset:22528
	ds_read_b128 v[92:95], v87 offset:23552
	s_waitcnt lgkmcnt(1)
	v_mfma_f32_32x32x16_bf16 v[16:31], v[72:75], v[68:71], v[16:31]
	ds_read_b128 v[72:75], v87 offset:30720
	ds_read_b128 v[96:99], v87 offset:31744
	s_waitcnt lgkmcnt(1)
	v_mfma_f32_32x32x16_bf16 v[0:15], v[72:75], v[68:71], v[0:15]
	ds_read_b128 v[72:75], v87 offset:6144
	ds_read_b128 v[100:103], v87 offset:7168
	s_waitcnt lgkmcnt(1)
	v_mfma_f32_32x32x16_bf16 v[48:63], v[72:75], v[68:71], v[48:63]
	ds_read_b128 v[72:75], v87 offset:14336
	ds_read_b128 v[104:107], v87 offset:15360
	s_waitcnt lgkmcnt(1)
	v_mfma_f32_32x32x16_bf16 v[32:47], v[72:75], v[68:71], v[32:47]
	v_lshlrev_b64 v[68:69], 13, v[108:109]
	v_ashrrev_i32_e32 v70, 2, v86
	v_lshlrev_b32_e32 v72, 5, v86
	v_and_b32_e32 v73, 4, v110
	v_and_or_b32 v68, v88, s23, v68
	v_ashrrev_i32_e32 v71, 31, v70
	v_and_b32_e32 v75, 0x60, v72
	v_mfma_f32_32x32x16_bf16 v[48:63], v[100:103], v[64:67], v[48:63]
	v_mul_u32_u24_e32 v72, 0x88, v73
	v_lshl_add_u64 v[68:69], v[68:69], 0, v[70:71]
	v_lshlrev_b32_e32 v74, 1, v91
	v_lshlrev_b32_e32 v71, 1, v72
	v_mad_u64_u32 v[72:73], s[50:51], v68, s42, v[82:83]
	v_and_or_b32 v74, v86, s22, v74
	v_mfma_f32_32x32x16_bf16 v[16:31], v[92:95], v[64:67], v[16:31]
	v_mad_i32_i24 v73, v69, s42, v73
	v_mul_lo_u32 v91, v70, s43
	v_lshlrev_b32_e32 v70, 2, v75
	v_add3_u32 v86, v146, v74, v71
	v_add3_u32 v71, v146, v71, v74
	v_lshl_add_u64 v[68:69], v[72:73], 0, v[84:85]
	v_lshlrev_b32_e32 v84, 1, v75
	v_mfma_f32_32x32x16_bf16 v[0:15], v[96:99], v[64:67], v[0:15]
	v_cvt_pk_bf16_f32 v48, v48, v49
	v_cvt_pk_bf16_f32 v49, v50, v51
	v_cvt_pk_bf16_f32 v50, v52, v53
	v_cvt_pk_bf16_f32 v51, v54, v55
	v_lshl_add_u64 v[68:69], v[68:69], 0, v[84:85]
	v_add_co_u32_e32 v102, vcc, s44, v68
	s_waitcnt lgkmcnt(0)
	v_mfma_f32_32x32x16_bf16 v[32:47], v[104:107], v[64:67], v[32:47]
	ds_read_b128 v[64:67], v87 offset:32768
	ds_read_b128 v[72:75], v87 offset:33792
	v_add3_u32 v91, v146, v91, v84
	v_addc_co_u32_e32 v103, vcc, 0, v69, vcc
	v_lshl_add_u64 v[100:101], v[68:69], 0, s[40:41]
	global_load_dwordx4 v[104:107], v[102:103], off offset:2048
	global_load_dwordx4 v[108:111], v[100:101], off offset:48
	global_load_dwordx4 v[112:115], v[100:101], off offset:32
	global_load_dwordx4 v[116:119], v[100:101], off offset:16
	v_add_u32_e32 v88, s2, v88
	s_nop 5
	v_cvt_pk_bf16_f32 v32, v32, v33
	s_waitcnt lgkmcnt(1)
	v_mfma_f32_32x32x16_bf16 v[16:31], v[64:67], v[48:51], v[16:31]
	ds_read_b128 v[52:55], v87 offset:36864
	ds_read_b128 v[64:67], v87 offset:37888
	ds_read_b128 v[92:95], v87 offset:38912
	ds_read_b128 v[96:99], v87 offset:39936
	v_cvt_pk_bf16_f32 v33, v34, v35
	v_cvt_pk_bf16_f32 v34, v36, v37
	v_cvt_pk_bf16_f32 v35, v38, v39
	v_cvt_pk_bf16_f32 v36, v40, v41
	v_cvt_pk_bf16_f32 v37, v42, v43
	v_cvt_pk_bf16_f32 v38, v44, v45
	s_waitcnt lgkmcnt(3)
	v_mfma_f32_32x32x16_bf16 v[0:15], v[52:55], v[48:51], v[0:15]
	v_cvt_pk_bf16_f32 v48, v56, v57
	v_cvt_pk_bf16_f32 v49, v58, v59
	v_cvt_pk_bf16_f32 v50, v60, v61
	v_cvt_pk_bf16_f32 v51, v62, v63
	v_cvt_pk_bf16_f32 v39, v46, v47
	s_waitcnt lgkmcnt(0)
	s_barrier
; DI bf16_t f2bf(float x) { return (bf16_t)(pk2(x, 0.f) & 0xffffu); }
; DI float bflo(unsigned u) { return __uint_as_float(u << 16); }
; DI float bfhi(unsigned u) { return __uint_as_float(u & 0xffff0000u); }
; DI int crow(int r, int hi) { return (r & 3) + 8 * (r >> 2) + 4 * hi; }
; #define MFMA32(a, b, c) __builtin_amdgcn_mfma_f32_32x32x16_bf16((a), (b), (c), 0, 0, 0)
; DI void gdn_out_unit(const Params& p, int U, char* lds) {
;     ...
;     for (int j2 = 0; j2 <= i2; ++j2)
; #pragma unroll
;       for (int s = 0; s < 2; ++s) o[i2] = MFMA32(*(const bf16x8*)(la + ((i2 * 2 + j2) * 2 + s) * 1024), Vb[j2][s], o[i2]);
;   __syncthreads();
; #pragma unroll
;   for (int i2 = 0; i2 < 2; ++i2)
; #pragma unroll
;     for (int r = 0; r < 16; ++r) ol[(32 * i2 + crow(r, hi)) * 136 + 32 * wv + r32] = f2bf(o[i2][r]);
;   __syncthreads();
;   {
;     const size_t t0 = (size_t)b * S_ + c * 64;
;     const int row = tid >> 2, q4 = tid & 3;
;     const bf16_t* gzp = proj + (t0 + row) * PP + 3072 + h * 128 + 32 * q4;
;     bf16_t* op = proj + (t0 + row) * PP + 1536 + h * 128 + 32 * q4;
;     float ss = 0.f;
; #pragma unroll
;     for (int q = 0; q < 4; ++q) { const u32x4 w = *(const u32x4*)(ol + row * 136 + 32 * q4 + 8 * q);
; #pragma unroll
;       for (int e = 0; e < 4; ++e) { const float a0 = bflo(w[e]), a1 = bfhi(w[e]); ss += a0 * a0 + a1 * a1; } }
	v_mfma_f32_32x32x16_bf16 v[0:15], v[64:67], v[48:51], v[0:15]
	v_mfma_f32_32x32x16_bf16 v[0:15], v[92:95], v[32:35], v[0:15]
	v_mfma_f32_32x32x16_bf16 v[16:31], v[72:75], v[48:51], v[16:31]
	v_mfma_f32_32x32x16_bf16 v[0:15], v[96:99], v[36:39], v[0:15]
	s_nop 10
	v_cvt_pk_bf16_f32 v16, v16, s0
	v_cvt_pk_bf16_f32 v17, v17, s0
	v_cvt_pk_bf16_f32 v18, v18, s0
	v_cvt_pk_bf16_f32 v19, v19, s0
	v_cvt_pk_bf16_f32 v20, v20, s0
	v_cvt_pk_bf16_f32 v21, v21, s0
	v_cvt_pk_bf16_f32 v22, v22, s0
	v_cvt_pk_bf16_f32 v23, v23, s0
	v_cvt_pk_bf16_f32 v26, v26, s0
	v_cvt_pk_bf16_f32 v27, v27, s0
	v_cvt_pk_bf16_f32 v28, v28, s0
	v_cvt_pk_bf16_f32 v29, v29, s0
	v_cvt_pk_bf16_f32 v0, v0, s0
	v_cvt_pk_bf16_f32 v1, v1, s0
	v_cvt_pk_bf16_f32 v2, v2, s0
	v_cvt_pk_bf16_f32 v3, v3, s0
	v_cvt_pk_bf16_f32 v4, v4, s0
	v_cvt_pk_bf16_f32 v5, v5, s0
	v_cvt_pk_bf16_f32 v6, v6, s0
	v_cvt_pk_bf16_f32 v7, v7, s0
	v_cvt_pk_bf16_f32 v8, v8, s0
	v_cvt_pk_bf16_f32 v9, v9, s0
	v_cvt_pk_bf16_f32 v10, v10, s0
	v_cvt_pk_bf16_f32 v11, v11, s0
	v_cvt_pk_bf16_f32 v12, v12, s0
	v_cvt_pk_bf16_f32 v13, v13, s0
	v_cvt_pk_bf16_f32 v14, v14, s0
	v_cvt_pk_bf16_f32 v15, v15, s0
	v_cvt_pk_bf16_f32 v24, v24, s0
	v_cvt_pk_bf16_f32 v25, v25, s0
	v_cvt_pk_bf16_f32 v30, v30, s0
	v_cvt_pk_bf16_f32 v31, v31, s0
	ds_write_b16 v86, v16 offset:40960
	ds_write_b16 v71, v17 offset:41232
	ds_write_b16 v71, v18 offset:41504
	ds_write_b16 v71, v19 offset:41776
	ds_write_b16 v71, v20 offset:43136
	ds_write_b16 v71, v21 offset:43408
	ds_write_b16 v71, v22 offset:43680
	ds_write_b16 v71, v23 offset:43952
	ds_write_b16 v71, v24 offset:45312
	ds_write_b16 v71, v25 offset:45584
	ds_write_b16 v71, v26 offset:45856
	ds_write_b16 v71, v27 offset:46128
	ds_write_b16 v71, v28 offset:47488
	ds_write_b16 v71, v29 offset:47760
	ds_write_b16 v71, v30 offset:48032
	ds_write_b16 v71, v31 offset:48304
	ds_write_b16 v71, v0 offset:49664
	ds_write_b16 v71, v1 offset:49936
	ds_write_b16 v71, v2 offset:50208
	ds_write_b16 v71, v3 offset:50480
	ds_write_b16 v71, v4 offset:51840
	ds_write_b16 v71, v5 offset:52112
	ds_write_b16 v71, v6 offset:52384
	ds_write_b16 v71, v7 offset:52656
	ds_write_b16 v71, v8 offset:54016
	ds_write_b16 v71, v9 offset:54288
	ds_write_b16 v71, v10 offset:54560
	ds_write_b16 v71, v11 offset:54832
	ds_write_b16 v71, v12 offset:56192
	ds_write_b16 v71, v13 offset:56464
	ds_write_b16 v71, v14 offset:56736
	ds_write_b16 v71, v15 offset:57008
	s_waitcnt lgkmcnt(0)
	s_barrier
	ds_read_b128 v[36:39], v91 offset:40960
	ds_read_b128 v[50:53], v91 offset:40976
	ds_read_b128 v[54:57], v91 offset:40992
	ds_read_b128 v[26:29], v91 offset:41008
	s_nop 1
	v_mov_b32_e32 v16, v216
	v_mov_b32_e32 v17, v217
	v_mov_b32_e32 v18, v218
	v_mov_b32_e32 v19, v219
	s_nop 1
	v_mov_b32_e32 v20, v212
	v_mov_b32_e32 v21, v213
	v_mov_b32_e32 v22, v214
	v_mov_b32_e32 v23, v215
	s_waitcnt lgkmcnt(3)
	v_lshlrev_b32_e32 v46, 16, v37
	v_and_b32_e32 v47, 0xffff0000, v37
	v_lshlrev_b32_e32 v58, 16, v36
	v_and_b32_e32 v59, 0xffff0000, v36
	v_lshlrev_b32_e32 v40, 16, v38
	v_and_b32_e32 v41, 0xffff0000, v38
	v_pk_mul_f32 v[64:65], v[46:47], v[46:47]
	v_pk_mul_f32 v[66:67], v[58:59], v[58:59]
	v_lshlrev_b32_e32 v34, 16, v39
	v_and_b32_e32 v35, 0xffff0000, v39
	v_pk_mul_f32 v[62:63], v[40:41], v[40:41]
	v_add_f32_e32 v64, v64, v65
	v_add_f32_e32 v65, v66, v67
	s_waitcnt lgkmcnt(2)
	v_lshlrev_b32_e32 v38, 16, v53
	v_and_b32_e32 v39, 0xffff0000, v53
	v_lshlrev_b32_e32 v42, 16, v52
	v_and_b32_e32 v43, 0xffff0000, v52
	v_lshlrev_b32_e32 v52, 16, v50
	v_and_b32_e32 v53, 0xffff0000, v50
	v_pk_mul_f32 v[60:61], v[34:35], v[34:35]
	v_add_f32_e32 v66, v62, v63
	v_add_f32_e32 v64, v65, v64
	v_lshlrev_b32_e32 v48, 16, v51
	v_and_b32_e32 v49, 0xffff0000, v51
	v_pk_mul_f32 v[92:93], v[52:53], v[52:53]
	v_add_f32_e32 v71, v60, v61
	v_add_f32_e32 v64, v66, v64
	v_pk_mul_f32 v[86:87], v[48:49], v[48:49]
	v_add_f32_e32 v67, v92, v93
	v_add_f32_e32 v64, v71, v64
	s_waitcnt lgkmcnt(1)
	v_lshlrev_b32_e32 v36, 16, v57
	v_and_b32_e32 v37, 0xffff0000, v57
	v_and_b32_e32 v51, 0xffff0000, v55
	v_and_b32_e32 v57, 0xffff0000, v54
	v_pk_mul_f32 v[74:75], v[42:43], v[42:43]
	v_add_f32_e32 v84, v86, v87
	v_add_f32_e32 v64, v67, v64
	v_lshlrev_b32_e32 v44, 16, v56
	v_and_b32_e32 v45, 0xffff0000, v56
	v_lshlrev_b32_e32 v50, 16, v55
	v_lshlrev_b32_e32 v56, 16, v54
	v_pk_mul_f32 v[72:73], v[38:39], v[38:39]
	v_mov_b32_e32 v100, v51
	v_mov_b32_e32 v101, v57
	v_add_f32_e32 v74, v74, v75
	v_add_f32_e32 v64, v84, v64
	v_mov_b32_e32 v98, v50
	v_mov_b32_e32 v99, v56
	v_pk_mul_f32 v[100:101], v[100:101], v[100:101]
	v_add_f32_e32 v72, v72, v73
	v_add_f32_e32 v64, v74, v64
	v_mov_b32_e32 v96, v37
	v_mov_b32_e32 v97, v45
	v_pk_fma_f32 v[62:63], v[98:99], v[98:99], v[100:101]
	v_add_f32_e32 v64, v72, v64
	v_mov_b32_e32 v94, v36
	v_mov_b32_e32 v95, v44
	v_pk_mul_f32 v[96:97], v[96:97], v[96:97]
	v_add_f32_e32 v63, v63, v64
	s_waitcnt lgkmcnt(0)
	v_lshlrev_b32_e32 v25, 16, v27
	v_lshlrev_b32_e32 v24, 16, v26
	v_and_b32_e32 v27, 0xffff0000, v27
	v_and_b32_e32 v26, 0xffff0000, v26
	v_pk_fma_f32 v[60:61], v[94:95], v[94:95], v[96:97]
	v_add_f32_e32 v62, v62, v63
	v_pk_mul_f32 v[32:33], v[26:27], v[26:27]
	v_add_f32_e32 v61, v61, v62
	v_lshlrev_b32_e32 v31, 16, v29
	v_lshlrev_b32_e32 v30, 16, v28
	v_and_b32_e32 v29, 0xffff0000, v29
	v_and_b32_e32 v28, 0xffff0000, v28
	v_pk_fma_f32 v[32:33], v[24:25], v[24:25], v[32:33]
	v_add_f32_e32 v60, v60, v61
	v_pk_mul_f32 v[54:55], v[28:29], v[28:29]
	v_add_f32_e32 v32, v32, v60
	v_pk_fma_f32 v[54:55], v[30:31], v[30:31], v[54:55]
	v_add_f32_e32 v32, v33, v32
	v_add_f32_e32 v32, v54, v32
	v_add_f32_e32 v32, v55, v32
	s_waitcnt vmcnt(3)
; DI unsigned pk2(float lo, float hi) { f32x2 v = {lo, hi}; bf16x2_t b = __builtin_convertvector(v, bf16x2_t); return __builtin_bit_cast(unsigned, b); }
; DI float bflo(unsigned u) { return __uint_as_float(u << 16); }
; DI float bfhi(unsigned u) { return __uint_as_float(u & 0xffff0000u); }
; DI float sigmoidf_(float x) { return __builtin_amdgcn_rcpf(1.f + __expf(-x)); }
; DI void gdn_out_unit(const Params& p, int U, char* lds) {
;     ...
;     ss += __uint_as_float((unsigned)__builtin_amdgcn_update_dpp(0, (int)__float_as_uint(ss), 0xB1, 0xF, 0xF, true));
;     ss += __uint_as_float((unsigned)__builtin_amdgcn_update_dpp(0, (int)__float_as_uint(ss), 0x4E, 0xF, 0xF, true));
;     const float rstd = rsqrtf(ss * (1.f / 128.f) + 1e-6f);
; #pragma unroll
;     for (int q = 0; q < 4; ++q) {
;       const u32x4 w = *(const u32x4*)(ol + row * 136 + 32 * q4 + 8 * q), gz = *(const u32x4*)(gzp + 8 * q);
;       const f32x4 n0 = *(const f32x4*)(p.gdn_norm_w + 32 * q4 + 8 * q), n1 = *(const f32x4*)(p.gdn_norm_w + 32 * q4 + 8 * q + 4);
;       float y[8];
; #pragma unroll
;       for (int e = 0; e < 4; ++e) { const float z0 = bflo(gz[e]), z1 = bfhi(gz[e]);
;         const float g0 = (2 * e < 4) ? n0[(2 * e) & 3] : n1[(2 * e) & 3], g1 = (2 * e + 1 < 4) ? n0[(2 * e + 1) & 3] : n1[(2 * e + 1) & 3];
;         y[2 * e] = bflo(w[e]) * rstd * g0 * (z0 * sigmoidf_(z0));
;         y[2 * e + 1] = bfhi(w[e]) * rstd * g1 * (z1 * sigmoidf_(z1)); }
;       u32x4 wv4 = {pk2(y[0], y[1]), pk2(y[2], y[3]), pk2(y[4], y[5]), pk2(y[6], y[7])};
;       *(u32x4*)(op + 8 * q) = wv4;
;     }
	v_mov_b32_e32 v12, v104
	v_mov_b32_e32 v13, v105
	v_mov_b32_e32 v14, v106
	v_mov_b32_e32 v15, v107
	v_lshlrev_b32_e32 v60, 16, v13
	v_and_b32_e32 v61, 0xffff0000, v13
	v_add_f32_dpp v32, v32, v32 quad_perm:[1,0,3,2] row_mask:0xf bank_mask:0xf bound_ctrl:1
	v_lshlrev_b32_e32 v62, 16, v12
	v_and_b32_e32 v63, 0xffff0000, v12
	v_add_f32_dpp v32, v32, v32 quad_perm:[2,3,0,1] row_mask:0xf bank_mask:0xf bound_ctrl:1
	v_fmamk_f32 v32, v32, 0x3c000000, v89
	v_mul_f32_e32 v33, 0x4b800000, v32
	v_cmp_gt_f32_e32 vcc, s45, v32
	v_lshlrev_b32_e32 v12, 16, v15
	v_and_b32_e32 v13, 0xffff0000, v15
	v_cndmask_b32_e32 v32, v32, v33, vcc
	v_rsq_f32_e32 v32, v32
	s_nop 0
	v_mul_f32_e32 v33, 0x45800000, v32
	v_cndmask_b32_e32 v32, v32, v33, vcc
	v_pk_mul_f32 v[54:55], v[32:33], v[58:59] op_sel_hi:[0,1]
	v_pk_mul_f32 v[46:47], v[32:33], v[46:47] op_sel_hi:[0,1]
	v_pk_mul_f32 v[40:41], v[32:33], v[40:41] op_sel_hi:[0,1]
	v_pk_mul_f32 v[34:35], v[32:33], v[34:35] op_sel_hi:[0,1]
	v_lshlrev_b32_e32 v58, 16, v14
	v_and_b32_e32 v59, 0xffff0000, v14
	s_waitcnt vmcnt(0)
	v_mov_b32_e32 v0, v108
	v_mov_b32_e32 v1, v109
	v_mov_b32_e32 v2, v110
	v_mov_b32_e32 v3, v111
	v_mov_b32_e32 v4, v112
	v_mov_b32_e32 v5, v113
	v_mov_b32_e32 v6, v114
	v_mov_b32_e32 v7, v115
	v_mov_b32_e32 v8, v116
	v_mov_b32_e32 v9, v117
	v_mov_b32_e32 v10, v118
	v_mov_b32_e32 v11, v119
	v_pk_mul_f32 v[14:15], v[20:21], v[54:55]
	v_pk_mul_f32 v[20:21], v[22:23], v[46:47]
	v_pk_mul_f32 v[16:17], v[16:17], v[40:41]
	v_pk_mul_f32 v[18:19], v[18:19], v[34:35]
	v_mul_f32_e32 v22, 0xbfb8aa3b, v58
	v_mul_f32_e32 v23, 0xbfb8aa3b, v59
	v_mul_f32_e32 v33, 0xbfb8aa3b, v60
	v_mul_f32_e32 v34, 0xbfb8aa3b, v61
	v_mul_f32_e32 v35, 0xbfb8aa3b, v62
	v_mul_f32_e32 v40, 0xbfb8aa3b, v63
	v_mul_f32_e32 v41, 0xbfb8aa3b, v12
	v_mul_f32_e32 v46, 0xbfb8aa3b, v13
	v_exp_f32_e32 v22, v22
	v_exp_f32_e32 v23, v23
	v_exp_f32_e32 v33, v33
	v_exp_f32_e32 v34, v34
	v_exp_f32_e32 v35, v35
	v_exp_f32_e32 v40, v40
	v_exp_f32_e32 v41, v41
	v_exp_f32_e32 v46, v46
	v_add_f32_e32 v22, 1.0, v22
	v_add_f32_e32 v23, 1.0, v23
	v_add_f32_e32 v33, 1.0, v33
	v_add_f32_e32 v47, 1.0, v34
	v_add_f32_e32 v54, 1.0, v35
	v_add_f32_e32 v55, 1.0, v40
	v_add_f32_e32 v64, 1.0, v41
	v_add_f32_e32 v65, 1.0, v46
	v_rcp_f32_e32 v22, v22
	v_rcp_f32_e32 v23, v23
	v_rcp_f32_e32 v34, v33
	v_rcp_f32_e32 v35, v47
	v_rcp_f32_e32 v40, v54
	v_rcp_f32_e32 v41, v55
	v_rcp_f32_e32 v46, v64
	v_rcp_f32_e32 v47, v65
	v_pk_mul_f32 v[22:23], v[22:23], v[58:59]
	v_pk_mul_f32 v[34:35], v[34:35], v[60:61]
	v_pk_mul_f32 v[40:41], v[40:41], v[62:63]
	v_pk_mul_f32 v[12:13], v[46:47], v[12:13]
	v_pk_mul_f32 v[14:15], v[40:41], v[14:15]
	v_pk_mul_f32 v[20:21], v[34:35], v[20:21]
	v_pk_mul_f32 v[16:17], v[22:23], v[16:17]
	v_pk_mul_f32 v[18:19], v[12:13], v[18:19]
	v_cvt_pk_bf16_f32 v12, v14, v15
	v_cvt_pk_bf16_f32 v13, v20, v21
	v_cvt_pk_bf16_f32 v14, v16, v17
	v_cvt_pk_bf16_f32 v15, v18, v19
	global_store_dwordx4 v[68:69], v[12:15], off offset:3072
	s_nop 1
	v_mov_b32_e32 v12, v220
	v_mov_b32_e32 v13, v221
	v_mov_b32_e32 v14, v222
	v_mov_b32_e32 v15, v223
	s_nop 0
	s_nop 1
	v_mov_b32_e32 v16, v224
	v_mov_b32_e32 v17, v225
	v_mov_b32_e32 v18, v226
	v_mov_b32_e32 v19, v227
	v_pk_mul_f32 v[34:35], v[32:33], v[42:43] op_sel_hi:[0,1]
	v_lshlrev_b32_e32 v40, 16, v10
	v_and_b32_e32 v41, 0xffff0000, v10
	v_lshlrev_b32_e32 v42, 16, v9
	v_and_b32_e32 v43, 0xffff0000, v9
	v_lshlrev_b32_e32 v46, 16, v8
	v_and_b32_e32 v47, 0xffff0000, v8
	v_lshlrev_b32_e32 v8, 16, v11
	v_and_b32_e32 v9, 0xffff0000, v11
	v_pk_mul_f32 v[20:21], v[32:33], v[52:53] op_sel_hi:[0,1]
	v_pk_mul_f32 v[22:23], v[32:33], v[48:49] op_sel_hi:[0,1]
	v_pk_mul_f32 v[38:39], v[32:33], v[38:39] op_sel_hi:[0,1]
	v_mul_f32_e32 v10, 0xbfb8aa3b, v40
	v_mul_f32_e32 v11, 0xbfb8aa3b, v41
	v_mul_f32_e32 v33, 0xbfb8aa3b, v42
	v_mul_f32_e32 v48, 0xbfb8aa3b, v43
	v_mul_f32_e32 v49, 0xbfb8aa3b, v46
	v_mul_f32_e32 v52, 0xbfb8aa3b, v47
	v_mul_f32_e32 v53, 0xbfb8aa3b, v8
	v_mul_f32_e32 v54, 0xbfb8aa3b, v9
	v_exp_f32_e32 v10, v10
	v_exp_f32_e32 v11, v11
	v_exp_f32_e32 v33, v33
	v_exp_f32_e32 v48, v48
	v_exp_f32_e32 v49, v49
	v_exp_f32_e32 v52, v52
	v_exp_f32_e32 v53, v53
	v_exp_f32_e32 v54, v54
	v_add_f32_e32 v10, 1.0, v10
	v_add_f32_e32 v11, 1.0, v11
	v_add_f32_e32 v33, 1.0, v33
	v_add_f32_e32 v55, 1.0, v48
	v_add_f32_e32 v58, 1.0, v49
	v_add_f32_e32 v59, 1.0, v52
	v_add_f32_e32 v60, 1.0, v53
	v_add_f32_e32 v61, 1.0, v54
	v_rcp_f32_e32 v10, v10
	v_rcp_f32_e32 v11, v11
	v_rcp_f32_e32 v48, v33
	v_rcp_f32_e32 v49, v55
	v_rcp_f32_e32 v52, v58
	v_rcp_f32_e32 v53, v59
	v_rcp_f32_e32 v54, v60
	v_rcp_f32_e32 v55, v61
	v_pk_mul_f32 v[10:11], v[10:11], v[40:41]
	v_pk_mul_f32 v[40:41], v[48:49], v[42:43]
	v_pk_mul_f32 v[42:43], v[52:53], v[46:47]
	v_pk_mul_f32 v[8:9], v[54:55], v[8:9]
	v_cmp_lt_i32_e32 vcc, s48, v90
	s_or_b64 s[10:11], vcc, s[10:11]
	v_pk_mul_f32 v[12:13], v[12:13], v[20:21]
	v_pk_mul_f32 v[14:15], v[14:15], v[22:23]
	v_pk_mul_f32 v[16:17], v[16:17], v[34:35]
	v_pk_mul_f32 v[18:19], v[18:19], v[38:39]
	v_pk_mul_f32 v[12:13], v[42:43], v[12:13]
; DI unsigned pk2(float lo, float hi) { f32x2 v = {lo, hi}; bf16x2_t b = __builtin_convertvector(v, bf16x2_t); return __builtin_bit_cast(unsigned, b); }
; DI float bflo(unsigned u) { return __uint_as_float(u << 16); }
; DI float bfhi(unsigned u) { return __uint_as_float(u & 0xffff0000u); }
; DI float sigmoidf_(float x) { return __builtin_amdgcn_rcpf(1.f + __expf(-x)); }
; DI void gdn_out_unit(const Params& p, int U, char* lds) {
;     ...
;     for (int q = 0; q < 4; ++q) {
;       const u32x4 w = *(const u32x4*)(ol + row * 136 + 32 * q4 + 8 * q), gz = *(const u32x4*)(gzp + 8 * q);
;       const f32x4 n0 = *(const f32x4*)(p.gdn_norm_w + 32 * q4 + 8 * q), n1 = *(const f32x4*)(p.gdn_norm_w + 32 * q4 + 8 * q + 4);
;       float y[8];
; #pragma unroll
;       for (int e = 0; e < 4; ++e) { const float z0 = bflo(gz[e]), z1 = bfhi(gz[e]);
;         const float g0 = (2 * e < 4) ? n0[(2 * e) & 3] : n1[(2 * e) & 3], g1 = (2 * e + 1 < 4) ? n0[(2 * e + 1) & 3] : n1[(2 * e + 1) & 3];
;         y[2 * e] = bflo(w[e]) * rstd * g0 * (z0 * sigmoidf_(z0));
;         y[2 * e + 1] = bfhi(w[e]) * rstd * g1 * (z1 * sigmoidf_(z1)); }
;       u32x4 wv4 = {pk2(y[0], y[1]), pk2(y[2], y[3]), pk2(y[4], y[5]), pk2(y[6], y[7])};
;       *(u32x4*)(op + 8 * q) = wv4;
;     }
	v_pk_mul_f32 v[14:15], v[40:41], v[14:15]
	v_pk_mul_f32 v[10:11], v[10:11], v[16:17]
	v_pk_mul_f32 v[16:17], v[8:9], v[18:19]
	v_cvt_pk_bf16_f32 v8, v12, v13
	v_cvt_pk_bf16_f32 v9, v14, v15
	v_cvt_pk_bf16_f32 v10, v10, v11
	v_cvt_pk_bf16_f32 v11, v16, v17
	global_store_dwordx4 v[68:69], v[8:11], off offset:3088
	s_nop 1
	v_mov_b32_e32 v8, v228
	v_mov_b32_e32 v9, v229
	v_mov_b32_e32 v10, v230
	v_mov_b32_e32 v11, v231
	s_nop 0
	s_nop 1
	v_mov_b32_e32 v12, v232
	v_mov_b32_e32 v13, v233
	v_mov_b32_e32 v14, v234
	v_mov_b32_e32 v15, v235
	v_pk_mul_f32 v[22:23], v[32:33], v[36:37] op_sel_hi:[0,1]
	v_lshlrev_b32_e32 v34, 16, v6
	v_and_b32_e32 v35, 0xffff0000, v6
	v_lshlrev_b32_e32 v36, 16, v5
	v_and_b32_e32 v37, 0xffff0000, v5
	v_lshlrev_b32_e32 v38, 16, v4
	v_and_b32_e32 v39, 0xffff0000, v4
	v_lshlrev_b32_e32 v4, 16, v7
	v_and_b32_e32 v5, 0xffff0000, v7
	v_pk_mul_f32 v[16:17], v[32:33], v[56:57] op_sel_hi:[0,1]
	v_pk_mul_f32 v[18:19], v[32:33], v[50:51] op_sel_hi:[0,1]
	v_pk_mul_f32 v[20:21], v[32:33], v[44:45] op_sel_hi:[0,1]
	v_mul_f32_e32 v6, 0xbfb8aa3b, v34
	v_mul_f32_e32 v7, 0xbfb8aa3b, v35
	v_mul_f32_e32 v33, 0xbfb8aa3b, v36
	v_mul_f32_e32 v40, 0xbfb8aa3b, v37
	v_mul_f32_e32 v41, 0xbfb8aa3b, v38
	v_mul_f32_e32 v42, 0xbfb8aa3b, v39
	v_mul_f32_e32 v43, 0xbfb8aa3b, v4
	v_mul_f32_e32 v44, 0xbfb8aa3b, v5
	v_exp_f32_e32 v6, v6
	v_exp_f32_e32 v7, v7
	v_exp_f32_e32 v33, v33
	v_exp_f32_e32 v40, v40
	v_exp_f32_e32 v41, v41
	v_exp_f32_e32 v42, v42
	v_exp_f32_e32 v43, v43
	v_exp_f32_e32 v44, v44
	v_add_f32_e32 v6, 1.0, v6
	v_add_f32_e32 v7, 1.0, v7
	v_add_f32_e32 v33, 1.0, v33
	v_add_f32_e32 v45, 1.0, v40
	v_add_f32_e32 v46, 1.0, v41
	v_add_f32_e32 v47, 1.0, v42
	v_add_f32_e32 v48, 1.0, v43
	v_add_f32_e32 v49, 1.0, v44
	v_rcp_f32_e32 v6, v6
	v_rcp_f32_e32 v7, v7
	v_rcp_f32_e32 v40, v33
	v_rcp_f32_e32 v41, v45
	v_rcp_f32_e32 v42, v46
	v_rcp_f32_e32 v43, v47
	v_rcp_f32_e32 v44, v48
	v_rcp_f32_e32 v45, v49
	v_pk_mul_f32 v[6:7], v[6:7], v[34:35]
	v_pk_mul_f32 v[34:35], v[40:41], v[36:37]
	v_pk_mul_f32 v[36:37], v[42:43], v[38:39]
	v_pk_mul_f32 v[4:5], v[44:45], v[4:5]
	v_pk_mul_f32 v[8:9], v[8:9], v[16:17]
	v_pk_mul_f32 v[10:11], v[10:11], v[18:19]
	v_pk_mul_f32 v[12:13], v[12:13], v[20:21]
	v_pk_mul_f32 v[14:15], v[14:15], v[22:23]
	v_pk_mul_f32 v[8:9], v[36:37], v[8:9]
	v_pk_mul_f32 v[10:11], v[34:35], v[10:11]
	v_pk_mul_f32 v[6:7], v[6:7], v[12:13]
	v_pk_mul_f32 v[12:13], v[4:5], v[14:15]
	v_cvt_pk_bf16_f32 v4, v8, v9
	v_cvt_pk_bf16_f32 v5, v10, v11
	v_cvt_pk_bf16_f32 v6, v6, v7
	v_cvt_pk_bf16_f32 v7, v12, v13
	global_store_dwordx4 v[68:69], v[4:7], off offset:3104
	s_nop 1
	v_mov_b32_e32 v4, v240
	v_mov_b32_e32 v5, v241
	v_mov_b32_e32 v6, v242
	v_mov_b32_e32 v7, v243
	s_nop 0
	s_nop 1
	v_mov_b32_e32 v8, v236
	v_mov_b32_e32 v9, v237
	v_mov_b32_e32 v10, v238
	v_mov_b32_e32 v11, v239
	v_mov_b32_e32 v14, v25
	v_mov_b32_e32 v25, v26
	v_mov_b32_e32 v13, v28
	v_mov_b32_e32 v28, v31
	v_pk_mul_f32 v[16:17], v[32:33], v[24:25] op_sel_hi:[0,1]
	v_lshlrev_b32_e32 v20, 16, v2
	v_and_b32_e32 v21, 0xffff0000, v2
	v_lshlrev_b32_e32 v22, 16, v1
	v_and_b32_e32 v23, 0xffff0000, v1
	v_lshlrev_b32_e32 v24, 16, v0
	v_and_b32_e32 v25, 0xffff0000, v0
	v_lshlrev_b32_e32 v0, 16, v3
	v_and_b32_e32 v1, 0xffff0000, v3
	v_mov_b32_e32 v12, v30
	v_mov_b32_e32 v15, v27
	v_pk_mul_f32 v[18:19], v[32:33], v[28:29] op_sel_hi:[0,1]
	v_mul_f32_e32 v2, 0xbfb8aa3b, v21
	v_mul_f32_e32 v3, 0xbfb8aa3b, v20
	v_mul_f32_e32 v26, 0xbfb8aa3b, v23
	v_mul_f32_e32 v27, 0xbfb8aa3b, v22
	v_mul_f32_e32 v28, 0xbfb8aa3b, v25
	v_mul_f32_e32 v29, 0xbfb8aa3b, v24
	v_mul_f32_e32 v30, 0xbfb8aa3b, v0
	v_mul_f32_e32 v31, 0xbfb8aa3b, v1
	v_exp_f32_e32 v2, v2
	v_exp_f32_e32 v3, v3
	v_exp_f32_e32 v26, v26
	v_exp_f32_e32 v27, v27
	v_exp_f32_e32 v28, v28
	v_exp_f32_e32 v29, v29
	v_exp_f32_e32 v30, v30
	v_exp_f32_e32 v31, v31
	v_pk_mul_f32 v[12:13], v[32:33], v[12:13] op_sel_hi:[0,1]
	v_pk_mul_f32 v[14:15], v[32:33], v[14:15] op_sel_hi:[0,1]
	v_add_f32_e32 v2, 1.0, v2
	v_add_f32_e32 v32, 1.0, v3
	v_add_f32_e32 v26, 1.0, v26
	v_add_f32_e32 v33, 1.0, v27
	v_add_f32_e32 v28, 1.0, v28
	v_add_f32_e32 v34, 1.0, v29
	v_add_f32_e32 v30, 1.0, v30
	v_add_f32_e32 v31, 1.0, v31
	v_rcp_f32_e32 v3, v2
	v_rcp_f32_e32 v2, v32
	v_rcp_f32_e32 v27, v26
	v_rcp_f32_e32 v26, v33
	v_rcp_f32_e32 v29, v28
	v_rcp_f32_e32 v28, v34
	v_rcp_f32_e32 v30, v30
	v_rcp_f32_e32 v31, v31
	v_pk_mul_f32 v[2:3], v[2:3], v[20:21]
	v_pk_mul_f32 v[20:21], v[26:27], v[22:23]
	v_pk_mul_f32 v[22:23], v[28:29], v[24:25]
	v_pk_mul_f32 v[0:1], v[30:31], v[0:1]
	v_pk_mul_f32 v[4:5], v[4:5], v[12:13]
	v_pk_mul_f32 v[10:11], v[10:11], v[14:15]
	v_pk_mul_f32 v[8:9], v[8:9], v[16:17]
	v_pk_mul_f32 v[6:7], v[6:7], v[18:19]
	v_pk_mul_f32 v[2:3], v[2:3], v[4:5]
	v_pk_mul_f32 v[4:5], v[20:21], v[10:11]
	v_pk_mul_f32 v[8:9], v[22:23], v[8:9]
	v_pk_mul_f32 v[6:7], v[0:1], v[6:7]
	v_cvt_pk_bf16_f32 v0, v8, v9
	v_cvt_pk_bf16_f32 v1, v4, v5
	v_cvt_pk_bf16_f32 v2, v2, v3
	v_cvt_pk_bf16_f32 v3, v6, v7
	global_store_dwordx4 v[68:69], v[0:3], off offset:3120
	s_andn2_b64 exec, exec, s[10:11]
	s_cbranch_execnz .LBB0_1336
